# v15 + DN GEMM walks its units in reverse order (starts with the ACT tiles GU wrote last, still in the memory-side cache)
# speedup vs baseline: 1.0089x; 1.0089x over previous
.LBB0_1779:
	v_ashrrev_i32_e32 v3, 31, v0
	v_lshrrev_b32_e32 v3, 26, v3
	v_lshlrev_b32_e32 v2, 4, v0
	v_add_u32_e32 v3, v0, v3
	v_bfe_i32 v0, v0, 27, 1
	v_lshrrev_b32_e32 v0, 22, v0
	v_add_u32_e32 v0, v2, v0
	v_and_b32_e32 v0, 0xfffffc00, v0
	v_sub_u32_e32 v0, v2, v0
	v_ashrrev_i32_e32 v11, 6, v3
	v_lshrrev_b32_e32 v3, 4, v0
	v_bitop3_b32 v0, v3, v0, 32 bitop3:0x6c
	v_ashrrev_i32_e32 v4, 31, v0
	s_add_u32 s51, s6, 0x9a000000
	v_readlane_b32 s4, v255, 4
	v_lshrrev_b32_e32 v4, 26, v4
	s_addc_u32 s52, s7, 0
	v_readlane_b32 s5, v255, 5
	s_lshl_b32 s28, s4, 15
	v_add_u32_e32 v4, v0, v4
	s_lshl_b64 s[4:5], s[28:29], 10
	v_lshlrev_b32_e32 v3, 3, v11
	v_ashrrev_i32_e32 v12, 6, v4
	v_and_b32_e32 v4, 0xc0, v4
	s_add_u32 s4, s6, s4
	v_and_b32_e32 v3, -16, v3
	v_sub_u32_e32 v0, v0, v4
	s_addc_u32 s5, s7, s5
	v_add_u32_e32 v3, v12, v3
	v_ashrrev_i16_sdwa v0, v228, sext(v0) dst_sel:DWORD dst_unused:UNUSED_PAD src0_sel:DWORD src1_sel:BYTE_0
	s_add_u32 s53, s4, 0x24400000
	v_lshlrev_b32_e32 v5, 5, v11
	v_bfe_i32 v13, v0, 0, 16
	v_lshlrev_b32_e32 v0, 1, v3
	v_lshrrev_b32_e32 v4, 2, v3
	v_and_b32_e32 v6, 3, v12
	s_mov_b32 s4, 0x3fffe0
	v_and_b32_e32 v5, 32, v5
	v_and_b32_e32 v0, 24, v0
	v_and_b32_e32 v4, 4, v4
	v_and_or_b32 v6, v3, s4, v6
	v_or3_b32 v0, v6, v4, v0
	v_add_lshl_u32 v4, v5, v13, 1
	v_add_u32_e32 v2, 0x2000, v2
	v_lshl_add_u32 v146, v3, 10, v4
	v_ashrrev_i32_e32 v3, 31, v2
	v_lshrrev_b32_e32 v3, 22, v3
	v_add_u32_e32 v3, v2, v3
	v_ashrrev_i32_e32 v14, 10, v3
	v_mul_i32_i24_e32 v3, 0x400, v14
	v_sub_u32_e32 v2, v2, v3
	v_lshrrev_b32_e32 v3, 4, v2
	v_bitop3_b32 v2, v3, v2, 32 bitop3:0x6c
	v_lshl_add_u32 v0, v0, 10, v4
	v_ashrrev_i32_e32 v4, 31, v2
	v_lshrrev_b32_e32 v4, 26, v4
	v_lshlrev_b32_e32 v3, 3, v14
	v_add_u32_e32 v4, v2, v4
	v_and_b32_e32 v3, -16, v3
	v_ashrrev_i32_e32 v15, 6, v4
	v_add_u32_e32 v3, v15, v3
	v_and_b32_e32 v6, 3, v15
	v_and_or_b32 v6, v3, s4, v6
	v_readlane_b32 s4, v253, 30
	s_addc_u32 s54, s5, 0
	s_add_i32 s4, s14, s4
	s_lshl_b32 s5, s27, 2
	s_sub_i32 s5, s5, 1
	s_sub_i32 s4, s5, s4
	s_ashr_i32 s5, s4, 31
	s_lshr_b32 s5, s5, 28
	v_and_b32_e32 v4, 0xc0, v4
	s_add_i32 s5, s4, s5
	v_sub_u32_e32 v2, v2, v4
	s_ashr_i32 s13, s5, 4
	v_ashrrev_i16_sdwa v2, v228, sext(v2) dst_sel:DWORD dst_unused:UNUSED_PAD src0_sel:DWORD src1_sel:BYTE_0
	s_lshl_b32 s14, s13, 2
	v_lshlrev_b32_e32 v5, 5, v14
	v_bfe_i32 v16, v2, 0, 16
	v_lshlrev_b32_e32 v2, 1, v3
	v_lshrrev_b32_e32 v4, 2, v3
	s_sub_i32 s13, s27, s14
	v_and_b32_e32 v5, 32, v5
	v_and_b32_e32 v2, 24, v2
	v_and_b32_e32 v4, 4, v4
	s_min_i32 s15, s13, 4
	v_or3_b32 v2, v6, v4, v2
	v_add_lshl_u32 v4, v5, v16, 1
	s_abs_i32 s20, s15
	v_lshl_add_u32 v148, v3, 10, v4
	v_cvt_f32_u32_e32 v3, s20
	v_lshl_add_u32 v150, v2, 10, v4
	s_sub_i32 s35, 0, s20
	s_andn2_b32 s5, s5, 15
	v_rcp_iflag_f32_e32 v2, v3
	s_sub_i32 s4, s4, s5
	s_abs_i32 s34, s4
	s_ashr_i32 s13, s46, 6
	v_mul_f32_e32 v2, 0x4f7ffffe, v2
	v_cvt_u32_f32_e32 v2, v2
	s_xor_b32 s5, s4, s15
	s_ashr_i32 s12, s46, 8
	s_lshl_b32 s21, s13, 10
	v_readfirstlane_b32 s38, v2
	s_mul_i32 s35, s35, s38
	s_mul_hi_u32 s35, s38, s35
	s_add_i32 s38, s38, s35
	s_mul_hi_u32 s35, s34, s38
	s_mul_i32 s38, s35, s20
	s_sub_i32 s34, s34, s38
	s_ashr_i32 s5, s5, 31
	s_add_i32 s38, s35, 1
	s_sub_i32 s39, s34, s20
	s_cmp_ge_u32 s34, s20
	s_cselect_b32 s35, s38, s35
	s_cselect_b32 s34, s39, s34
	s_add_i32 s38, s35, 1
	v_mbcnt_lo_u32_b32 v2, -1, 0
	v_mbcnt_hi_u32_b32 v2, -1, v2
	s_cmp_ge_u32 s34, s20
	v_and_b32_e32 v2, 31, v2
	s_cselect_b32 s20, s38, s35
	v_lshl_add_u32 v3, v2, 2, s31
	s_xor_b32 s20, s20, s5
	ds_read_b32 v3, v3 offset:4
	s_sub_i32 s40, s20, s5
	s_mul_i32 s5, s40, s15
	s_sub_i32 s4, s4, s5
	s_add_i32 s38, s14, s4
	v_cmp_ne_u32_e32 vcc, 31, v2
	s_waitcnt lgkmcnt(0)
	v_cmp_ge_i32_e64 s[4:5], s38, v3
	s_and_b64 s[4:5], vcc, s[4:5]
	s_ashr_i32 s39, s38, 31
	v_cndmask_b32_e64 v2, 0, 1, s[4:5]
	v_cmp_ne_u32_e32 vcc, 0, v2
	s_bcnt1_i32_b32 s20, vcc_lo
	s_ashr_i32 s41, s40, 31
	s_lshl_b64 s[14:15], s[38:39], 18
	s_lshl_b64 s[4:5], s[40:41], 18
	s_lshl_b32 s20, s20, 20
	s_add_u32 s4, s53, s4
	s_addc_u32 s5, s54, s5
	s_add_u32 s42, s4, s20
	s_addc_u32 s43, s5, 0
	s_add_i32 s55, s21, 0
	s_add_i32 s56, s55, 0x10000
	s_add_i32 s57, s55, 0x12000
	s_mov_b32 m0, s56
	s_add_u32 s44, s51, s14
	global_load_lds_dwordx4 v0, s[42:43]
	s_mov_b32 m0, s57
	s_addc_u32 s45, s52, s15
	s_add_i32 s58, s55, 0x2000
	global_load_lds_dwordx4 v150, s[42:43]
	s_mov_b32 m0, s55
	s_add_u32 s4, s42, 0x20000
	global_load_lds_dwordx4 v146, s[44:45]
	s_mov_b32 m0, s58
	s_addc_u32 s5, s43, 0
	s_add_i32 s59, s55, 0x14000
	global_load_lds_dwordx4 v148, s[44:45]
	s_mov_b32 m0, s59
	s_add_i32 s60, s55, 0x16000
	global_load_lds_dwordx4 v0, s[4:5]
	s_mov_b32 m0, s60
	v_mov_b32_e32 v151, v1
	global_load_lds_dwordx4 v150, s[4:5]
	s_add_u32 s4, s44, 0x20000
	s_addc_u32 s5, s45, 0
	s_add_i32 s61, s55, 0x4000
	s_mov_b32 m0, s61
	s_add_i32 s62, s55, 0x6000
	global_load_lds_dwordx4 v146, s[4:5]
	s_mov_b32 m0, s62
	v_mov_b32_e32 v147, v1
	global_load_lds_dwordx4 v148, s[4:5]
	v_mov_b32_e32 v149, v1
	v_lshl_add_u64 v[8:9], s[42:43], 0, v[0:1]
	v_lshl_add_u64 v[6:7], s[42:43], 0, v[150:151]
	v_lshl_add_u64 v[4:5], s[44:45], 0, v[146:147]
	s_cmp_lg_u32 s12, 1
	v_lshl_add_u64 v[2:3], s[44:45], 0, v[148:149]
	s_cbranch_scc1 .LBB0_1781
	s_barrier

.LBB0_1788:
	s_ashr_i32 s8, s14, 3
	s_add_i32 s8, s20, s8
	s_lshl_b32 s9, s27, 2
	s_sub_i32 s9, s9, 1
	s_sub_i32 s8, s9, s8
	s_ashr_i32 s9, s8, 31
	s_lshr_b32 s9, s9, 28
	s_add_i32 s9, s8, s9
	s_ashr_i32 s14, s9, 4
	s_lshl_b32 s15, s14, 2
	s_sub_i32 s14, s27, s15
	s_min_i32 s20, s14, 4
	s_abs_i32 s14, s20
	v_cvt_f32_u32_e32 v2, s14
	s_sub_i32 s34, 0, s14
	s_andn2_b32 s9, s9, 15
	s_sub_i32 s8, s8, s9
	v_rcp_iflag_f32_e32 v2, v2
	s_abs_i32 s9, s8
	s_xor_b32 s21, s8, s20
	s_ashr_i32 s21, s21, 31
	v_mul_f32_e32 v2, 0x4f7ffffe, v2
	v_cvt_u32_f32_e32 v2, v2
	s_nop 0
	v_readfirstlane_b32 s35, v2
	s_mul_i32 s34, s34, s35
	s_mul_hi_u32 s34, s35, s34
	s_add_i32 s35, s35, s34
	s_mul_hi_u32 s34, s9, s35
	s_mul_i32 s35, s34, s14
	s_sub_i32 s9, s9, s35
	s_add_i32 s39, s34, 1
	s_sub_i32 s35, s9, s14
	s_cmp_ge_u32 s9, s14
	s_cselect_b32 s34, s39, s34
	s_cselect_b32 s9, s35, s9
	s_add_i32 s35, s34, 1
	s_cmp_ge_u32 s9, s14
	s_cselect_b32 s9, s35, s34
	s_xor_b32 s9, s9, s21
	s_sub_i32 s14, s9, s21
	s_mul_i32 s9, s14, s20
	s_sub_i32 s8, s8, s9
	s_add_i32 s20, s15, s8
